# SSD chain: the per-chunk scalar kernarg pointer load (dt base select) hoisted out of the 32-chunk loop (two pointers loaded once per task, selected per chunk)
# baseline (speedup 1.0000x reference)
; __device__ __forceinline__ int opaque_tid() { int t = threadIdx.x; asm volatile("" : "+v"(t)); return t; }
; __device__ void ssd_task(KParams& p, int task, char* smem) {
;   const int dir = task & 1, ph = (task >> 1) & 1, h = (task >> 2) & 15, b = task >> 6;
;   const int tid = opaque_tid(), lane = tid & 63, w = tid >> 6;
;   const int g = h >> 3, lr0 = lane & 15, lq0 = lane >> 4;
;   const float a = -__expf(dir ? p.a_log_b[h] : p.a_log_f[h]);
;   char* sCc = smem; char* sBc = smem + 16384; char* sBT = smem + 32768; char* sXT = smem + 49152; char* sHb = smem + 57344;
;   float* se = reinterpret_cast<float*>(smem + 73728);
;   float* sdt = se + 64; float* sw = se + 128; float* sy = se + 192; float* stot = se + 256;
;   bf16_t* yo = reinterpret_cast<bf16_t*>(dir ? p.yb : p.yf);
;   f32x4 H[2][2];
; #pragma unroll
;   for (int i = 0; i < 2; ++i)
; #pragma unroll
;     for (int j = 0; j < 2; ++j) H[i][j] = f32x4{0.f, 0.f, 0.f, 0.f};
;   __syncthreads();
;   for (int i = tid; i < 512; i += NTHREADS) reinterpret_cast<uint4*>(sHb)[i] = uint4{0, 0, 0, 0};
;   const int crow = tid >> 4, cch = tid & 15;
;   const int trow = tid >> 3, tch = tid & 7;
;   uint4 rC0, rC1, rC2, rC3, rB0, rB1, rB2, rB3, rT0, rT1, rT2, rT3, rX;
;   rC0 = rC1 = rC2 = rC3 = rB0 = rB1 = rB2 = rB3 = uint4{0, 0, 0, 0};
;   float rdt = 0.f;
;     ...
;   SSD_PREFETCH(0);
.LBB0_739:
	s_or_b64 exec, exec, s[10:11]
	s_mul_i32 s11, s38, 0xa0000
	s_mul_hi_i32 s10, s38, 0xa0000
	s_add_u32 s11, s24, s11
	s_addc_u32 s37, s25, s10
	s_lshl_b32 s10, s40, 1
	s_add_u32 s10, s11, s10
	s_addc_u32 s11, s37, 0
	s_lshl_b32 s37, s28, 4
	v_ashrrev_i32_e32 v7, 3, v98
	s_and_b32 s37, s37, 0x80
	v_add_u32_e32 v2, s37, v7
	v_add_u32_e32 v102, 0x400, v2
	v_ashrrev_i32_e32 v103, 31, v102
	v_lshlrev_b32_e32 v4, 3, v98
	v_lshlrev_b64 v[2:3], 9, v[102:103]
	v_and_b32_e32 v8, 56, v4
	v_lshl_add_u64 v[2:3], s[10:11], 0, v[2:3]
	v_lshlrev_b32_e32 v4, 1, v8
	v_mov_b32_e32 v5, v99
	v_lshl_add_u64 v[2:3], v[2:3], 0, v[4:5]
	v_add_co_u32_e32 v10, vcc, s67, v2
	s_lshl_b32 s41, s75, 4
	s_nop 0
	v_addc_co_u32_e32 v11, vcc, 0, v3, vcc
	global_load_dwordx4 v[38:41], v[2:3], off
	global_load_dwordx4 v[42:45], v[10:11], off
	v_add_co_u32_e32 v10, vcc, s68, v2
	s_lshl_b32 s40, s28, 6
	s_and_b32 s54, s41, 32
	v_addc_co_u32_e32 v11, vcc, 0, v3, vcc
	s_or_b32 s40, s40, s54
	v_add_co_u32_e32 v2, vcc, s69, v2
	v_add_u32_e32 v104, s40, v7
	s_nop 0
	v_addc_co_u32_e32 v3, vcc, 0, v3, vcc
	v_ashrrev_i32_e32 v105, 31, v104
	global_load_dwordx4 v[46:49], v[10:11], off
	global_load_dwordx4 v[50:53], v[2:3], off
	v_lshlrev_b64 v[2:3], 9, v[104:105]
	v_lshl_add_u64 v[2:3], s[10:11], 0, v[2:3]
	v_lshl_add_u64 v[2:3], v[2:3], 0, v[4:5]
	global_load_dwordx4 v[54:57], v[2:3], off
	s_lshl_b64 s[42:43], s[38:39], 11
	s_and_b64 s[52:53], s[6:7], exec
	v_and_b32_e32 v3, 63, v98
	s_cselect_b32 s76, s63, s47
	s_cselect_b32 s77, s62, s46
	s_lshl_b32 s37, s37, 1
	v_ashrrev_i32_e32 v2, 4, v98
	v_lshlrev_b32_e32 v4, 2, v3
	s_add_u32 s52, s16, s37
	v_or_b32_e32 v127, 0x12000, v4
	v_or_b32_e32 v128, 0x12100, v4
	v_or_b32_e32 v129, 0x12200, v4
	v_or_b32_e32 v130, 0x12300, v4
	v_xor_b32_e32 v4, v2, v98
	s_addc_u32 s53, s17, 0
	s_lshl_b32 s28, s28, 7
	v_cmp_eq_u32_e64 s[10:11], 0, v3
	v_lshlrev_b32_e32 v3, 8, v2
	v_lshlrev_b32_e32 v4, 4, v4
	s_add_u32 s28, s50, s28
	v_and_or_b32 v131, v4, s70, v3
	v_xor_b32_e32 v4, v7, v98
	s_addc_u32 s37, s51, 0
	s_lshl_b32 s50, s54, 1
	v_and_b32_e32 v125, 15, v98
	v_lshlrev_b32_e32 v3, 7, v7
	v_lshlrev_b32_e32 v4, 4, v4
	s_add_u32 s50, s28, s50
	v_and_or_b32 v132, v4, s71, v3
	v_lshlrev_b32_e32 v4, 4, v125
	s_addc_u32 s51, s37, 0
	v_lshl_add_u64 v[106:107], s[52:53], 0, v[4:5]
	v_and_b32_e32 v4, 0xffffffc0, v98
	s_and_b64 s[52:53], s[6:7], exec
	v_ashrrev_i32_e32 v3, 31, v2
	v_add_u32_e32 v134, 0x12000, v4
	v_add_u32_e32 v138, 0x12300, v4
	s_cselect_b32 s28, s72, 0x1d8
	v_mov_b32_e32 v4, v99
	v_ashrrev_i32_e32 v9, 6, v98
	s_add_u32 s78, s26, s28
	v_lshl_add_u64 v[108:109], s[42:43], 0, v[2:3]
	v_mov_b32_e32 v2, v99
	v_mov_b32_e32 v3, v99
	v_mov_b64_e32 v[16:17], v[4:5]
	v_mov_b64_e32 v[24:25], v[4:5]
	v_mov_b64_e32 v[32:33], v[4:5]
	v_mov_b64_e32 v[12:13], v[4:5]
	v_mov_b64_e32 v[20:21], v[4:5]
	v_mov_b64_e32 v[28:29], v[4:5]
	v_mov_b64_e32 v[36:37], v[4:5]
	s_mul_hi_i32 s41, s38, 0x500
	s_mul_i32 s40, s38, 0x500
	v_bfe_u32 v126, v98, 4, 2
	v_lshlrev_b32_e32 v133, 12, v9
	v_lshlrev_b32_e32 v136, 4, v9
	v_lshlrev_b32_e32 v137, 11, v9
	v_lshlrev_b32_e32 v139, 5, v9
	s_addc_u32 s79, s27, 0
	s_mov_b32 s86, s77
	s_mov_b32 s87, s76
	s_load_dwordx2 s[88:89], s[86:87], 0x0
	s_load_dwordx2 s[90:91], s[78:79], 0x0
	s_mov_b32 s80, -4
	v_lshlrev_b32_e32 v98, 1, v8
	v_mov_b64_e32 v[14:15], v[2:3]
	v_mov_b64_e32 v[22:23], v[2:3]
	v_mov_b64_e32 v[30:31], v[2:3]
	v_mov_b64_e32 v[10:11], v[2:3]
	v_mov_b64_e32 v[18:19], v[2:3]
	v_mov_b64_e32 v[26:27], v[2:3]
	v_mov_b64_e32 v[34:35], v[2:3]
	v_mov_b32_e32 v7, v6
	v_mov_b32_e32 v8, v6
	v_mov_b32_e32 v9, v6
	v_mov_b32_e32 v58, v6
	v_mov_b32_e32 v59, v6
	v_mov_b32_e32 v60, v6
	v_mov_b32_e32 v61, v6
	v_mov_b32_e32 v66, v6
	v_mov_b32_e32 v67, v6
	v_mov_b32_e32 v68, v6
	v_mov_b32_e32 v69, v6
	v_mov_b32_e32 v62, v6
	v_mov_b32_e32 v63, v6
	v_mov_b32_e32 v64, v6
	v_mov_b32_e32 v65, v6
	s_branch .LBB0_741

; __device__ void ssd_task(KParams& p, int task, char* smem) {
;     ...
;       const int ot = swz8(trow, tch);
;       *reinterpret_cast<uint4*>(sBT + ot) = rT0;
;       *reinterpret_cast<uint4*>(sBT + ot + 4096) = rT1;
;       *reinterpret_cast<uint4*>(sBT + ot + 8192) = rT2;
;       *reinterpret_cast<uint4*>(sBT + ot + 12288) = rT3;
;       *reinterpret_cast<uint4*>(sXT + ot) = rX;
;     }
;     if (step + 1 < 36) SSD_PREFETCH(step + 1);
.LBB0_750:
	s_cmp_eq_u32 s80, 31
	s_waitcnt vmcnt(4)
	ds_write_b128 v132, v[38:41] offset:32768
	s_waitcnt vmcnt(3)
	ds_write_b128 v132, v[42:45] offset:36864
	s_waitcnt vmcnt(2)
	ds_write_b128 v132, v[46:49] offset:40960
	s_waitcnt vmcnt(1)
	ds_write_b128 v132, v[50:53] offset:45056
	s_waitcnt vmcnt(0)
	ds_write_b128 v132, v[54:57] offset:49152
	s_cbranch_scc1 .LBB0_756
	s_add_i32 s37, s80, 5
	s_cmp_lt_u32 s28, 3
	s_cselect_b64 s[54:55], -1, 0
	s_cmp_gt_u32 s28, 2
	s_cselect_b64 s[58:59], -1, 0
	s_add_i32 s28, s80, 1
	s_and_b64 s[56:57], s[54:55], exec
	s_cselect_b32 s28, s37, s28
	s_cselect_b32 s37, 3, 31
	s_sub_i32 s37, s37, s28
	s_and_b64 s[56:57], s[6:7], exec
	s_cselect_b32 s28, s28, s37
	s_lshl_b32 s56, s28, 6
	s_ashr_i32 s57, s56, 31
	s_and_b64 s[60:61], s[54:55], exec
	s_cselect_b32 s28, 8, 11
	s_and_saveexec_b64 s[60:61], s[8:9]
	s_cbranch_execz .LBB0_753
	s_and_b64 s[82:83], s[54:55], exec
	s_cselect_b32 s83, s89, s91
	s_cselect_b32 s82, s88, s90
	s_lshl_b64 s[84:85], s[38:39], s28
	s_add_u32 s84, s56, s84
	s_addc_u32 s85, s57, s85
	v_lshl_add_u64 v[38:39], s[84:85], 0, v[100:101]
	v_lshlrev_b64 v[38:39], 6, v[38:39]
	s_waitcnt lgkmcnt(0)
	v_lshl_add_u64 v[38:39], s[82:83], 0, v[38:39]
	s_mov_b32 s37, s29
	v_lshl_add_u64 v[38:39], v[38:39], 0, s[36:37]
	global_load_dword v124, v[38:39], off
